# dead have-checks removed from both MoE converter paths (pre-converted groups no longer have producer items)
# speedup vs baseline: 1.0166x; 1.0031x over previous
; __device__ __forceinline__ int lane_id() { int r; asm volatile("v_mbcnt_lo_u32_b32 %0, -1, 0\n\tv_mbcnt_hi_u32_b32 %0, -1, %0" : "=v"(r)); return r; }
; #define CI_LOAD(R, kt) do { _Pragma("unroll") for (int _j = 0; _j < 16; ++_j) R[_j] = __builtin_nontemporal_load((const f32x4*)(src + (size_t)((kt) * 128 + _j) * LDB)); } while (0)
; __device__ __forceinline__ int ld_now(const int* ptr) { int r = ld_early(ptr); LD_WAIT(r); return r; }
; template <int LDB>
; __device__ __forceinline__ void convert_image(const float* __restrict__ W, int col0, int col1, unsigned char* __restrict__ img, LAS3 char* lds, int wid) {
;     int lane = lane_id(); asm volatile("" : "+v"(lane));
;     const int n4 = lane, half = n4 >> 5, nloc = (n4 & 31) * 4;
;     const float* src = W + (size_t)(wid * 16) * LDB + ((n4 < 32) ? col0 + n4 * 4 : col1 + (n4 - 32) * 4);
;     const unsigned cpo = (unsigned)(wid * 4096 + lane * 16);
;     ...
;     f32x4 ra[16], rb[16];
;     CI_LOAD(ra, 0);
; template <int EPI>
; __device__ __forceinline__ int* moe_phase(const Params& p, LAS3 char* lds, int wid, int* pend_in) {
;     ...
;                     if (conv) {
;                         const bool have = (EPI == 3) && (__builtin_amdgcn_readfirstlane(ld_now(sy.flag)) != 0);
;                         if (have) { }
;                         else if (EPI == 2) convert_image<2 * DFF>(p.w_gate_up + (size_t)e * D * (2 * DFF), pn * 128, DFF + pn * 128, img, lds, wid);
;                         else convert_image<D>(p.w_down + (size_t)e * DFF * D, pn * 256, pn * 256 + 128, img, lds, wid);
.LBB0_586:
	s_and_b64 vcc, exec, s[0:1]
	s_cbranch_vccz .LBB0_520
	v_mbcnt_lo_u32_b32 v66, -1, 0
	v_mbcnt_hi_u32_b32 v66, -1, v66
	s_lshl_b32 s4, s12, 11
	s_lshl_b64 s[30:31], s[4:5], 13
	v_lshlrev_b32_e32 v67, 2, v66
	v_readlane_b32 s0, v255, 4
	v_lshl_add_u32 v0, s15, 8, v67
	s_add_u32 s0, s0, s30
	v_readlane_b32 s1, v255, 6
	v_ashrrev_i32_e32 v1, 31, v0
	s_addc_u32 s1, s1, s31
	v_lshlrev_b64 v[64:65], 2, v[0:1]
	v_lshl_add_u64 v[132:133], s[0:1], 0, v[64:65]
	s_waitcnt vmcnt(14)
	v_add_co_u32_e32 v4, vcc, s20, v132
	v_lshlrev_b32_e32 v68, 9, v66
	s_nop 0
	v_addc_co_u32_e32 v5, vcc, 0, v133, vcc
	s_waitcnt vmcnt(13)
	v_add_co_u32_e32 v8, vcc, s21, v132
	global_load_dwordx4 v[0:3], v[132:133], off nt
	s_nop 0
	global_load_dwordx4 v[4:7], v[4:5], off nt
	v_addc_co_u32_e32 v9, vcc, 0, v133, vcc
	s_waitcnt vmcnt(14)
	v_add_co_u32_e32 v12, vcc, s22, v132
	v_and_b32_e32 v68, 0xffffc000, v68
	s_nop 0
	v_addc_co_u32_e32 v13, vcc, 0, v133, vcc
	s_waitcnt vmcnt(13)
	v_add_co_u32_e32 v16, vcc, s23, v132
	global_load_dwordx4 v[8:11], v[8:9], off nt
	s_nop 0
	global_load_dwordx4 v[12:15], v[12:13], off nt
	v_addc_co_u32_e32 v17, vcc, 0, v133, vcc
	s_waitcnt vmcnt(14)
	v_add_co_u32_e32 v20, vcc, s86, v132
	v_and_b32_e32 v67, 0x7c, v67
	s_nop 0
	v_addc_co_u32_e32 v21, vcc, 0, v133, vcc
	s_waitcnt vmcnt(13)
	v_add_co_u32_e32 v24, vcc, s87, v132
	global_load_dwordx4 v[16:19], v[16:17], off nt
	s_nop 0
	global_load_dwordx4 v[20:23], v[20:21], off nt
	v_addc_co_u32_e32 v25, vcc, 0, v133, vcc
	s_waitcnt vmcnt(14)
	v_add_co_u32_e32 v28, vcc, s95, v132
	v_add_u32_e32 v68, 0, v68
	s_nop 0
	v_addc_co_u32_e32 v29, vcc, 0, v133, vcc
	s_waitcnt vmcnt(13)
	v_add_co_u32_e32 v32, vcc, s8, v132
	global_load_dwordx4 v[24:27], v[24:25], off nt
	s_nop 0
	global_load_dwordx4 v[28:31], v[28:29], off nt
	v_addc_co_u32_e32 v33, vcc, 0, v133, vcc
	s_waitcnt vmcnt(14)
	v_add_co_u32_e32 v36, vcc, s97, v132
	v_lshlrev_b32_e32 v136, 4, v66
	s_nop 0
	v_addc_co_u32_e32 v37, vcc, 0, v133, vcc
	s_waitcnt vmcnt(13)
	v_add_co_u32_e32 v40, vcc, s98, v132
	global_load_dwordx4 v[32:35], v[32:33], off nt
	s_nop 0
	global_load_dwordx4 v[36:39], v[36:37], off nt
	v_addc_co_u32_e32 v41, vcc, 0, v133, vcc
	s_waitcnt vmcnt(14)
	v_add_co_u32_e32 v44, vcc, s99, v132
	v_readlane_b32 s0, v254, 56
	s_nop 0
	v_addc_co_u32_e32 v45, vcc, 0, v133, vcc
	s_waitcnt vmcnt(13)
	v_add_co_u32_e32 v48, vcc, s18, v132
	global_load_dwordx4 v[40:43], v[40:41], off nt
	s_nop 0
	global_load_dwordx4 v[44:47], v[44:45], off nt
	v_addc_co_u32_e32 v49, vcc, 0, v133, vcc
	s_waitcnt vmcnt(14)
	v_add_co_u32_e32 v52, vcc, s7, v132
	v_lshl_add_u32 v69, v67, 7, v68
	s_nop 0
	v_addc_co_u32_e32 v53, vcc, 0, v133, vcc
	s_waitcnt vmcnt(13)
	v_add_co_u32_e32 v56, vcc, s9, v132
	global_load_dwordx4 v[48:51], v[48:49], off nt
	s_nop 0
	global_load_dwordx4 v[52:55], v[52:53], off nt
	v_addc_co_u32_e32 v57, vcc, 0, v133, vcc
	s_waitcnt vmcnt(14)
	v_add_co_u32_e32 v60, vcc, s16, v132
	v_or_b32_e32 v70, 2, v67
	s_nop 0
	v_addc_co_u32_e32 v61, vcc, 0, v133, vcc
	global_load_dwordx4 v[56:59], v[56:57], off nt
	s_nop 0
	global_load_dwordx4 v[60:63], v[60:61], off nt
	v_or_b32_e32 v67, 3, v67
	v_add_u32_e32 v137, s0, v136
	v_lshlrev_b32_e32 v66, 1, v66
	v_readlane_b32 s0, v254, 0
	v_lshl_add_u32 v71, v70, 7, v68
	v_lshrrev_b32_e32 v70, 1, v70
	v_lshl_add_u32 v68, v67, 7, v68
	v_lshrrev_b32_e32 v67, 1, v67
	v_bitop3_b32 v66, v66, s0, 6 bitop3:0x6c
	v_bitop3_b32 v70, v70, s0, 7 bitop3:0x6c
	v_bitop3_b32 v67, v67, s0, 7 bitop3:0x6c
	s_lshl_b32 s0, s14, 3
	s_and_b32 s0, s0, 0xc0
	s_lshl_b32 s1, s19, 3
	s_add_i32 s0, s0, s1
	s_or_b32 s4, s0, s15
	v_readlane_b32 s36, v254, 20
	s_lshl_b64 s[0:1], s[4:5], 19
	v_readlane_b32 s44, v254, 28
	v_readlane_b32 s45, v254, 29
	s_add_u32 s0, s44, s0
	s_addc_u32 s1, s45, s1
	v_readlane_b32 s4, v255, 5
	s_add_u32 s14, s4, s30
	v_readlane_b32 s4, v255, 7
	v_lshlrev_b32_e32 v66, 4, v66
	v_lshlrev_b32_e32 v70, 4, v70
	v_lshlrev_b32_e32 v67, 4, v67
	s_addc_u32 s15, s4, s31
	v_add_u32_e32 v138, 0x400, v137
	v_add_u32_e32 v139, 0x800, v137
	v_add_u32_e32 v140, 0xc00, v137
	v_lshl_add_u64 v[134:135], s[14:15], 0, v[64:65]
	s_mov_b32 s14, -2
	v_add_u32_e32 v141, v69, v66
	v_add_u32_e32 v142, v71, v70
	v_add_u32_e32 v143, v68, v67
	v_readlane_b32 s37, v254, 21
	v_readlane_b32 s38, v254, 22
	v_readlane_b32 s39, v254, 23
	v_readlane_b32 s40, v254, 24
	v_readlane_b32 s41, v254, 25
	v_readlane_b32 s42, v254, 26
	v_readlane_b32 s43, v254, 27
	v_readlane_b32 s46, v254, 30
	v_readlane_b32 s47, v254, 31
	v_readlane_b32 s48, v254, 32
	v_readlane_b32 s49, v254, 33
	v_readlane_b32 s50, v254, 34
	v_readlane_b32 s51, v254, 35
